# e2_earlybar1
# baseline (speedup 1.0000x reference)
.LBB2_31:
	s_add_i32 s31, s35, 0x80
	s_add_u32 s46, s8, s31
	s_addc_u32 s47, s9, 0
	s_add_i32 s31, s35, 0x100
	s_and_b64 s[40:41], s[38:39], exec
	s_cselect_b32 s31, s90, s31
	s_add_u32 s42, s8, s31
	s_addc_u32 s43, s9, 0
	s_add_i32 s31, s93, 0x100
	s_and_b64 s[40:41], s[38:39], exec
	s_cselect_b32 s31, s88, s31
	s_add_u32 s44, s8, s31
	s_addc_u32 s45, s9, 0
	s_add_i32 s31, s90, 0x80
	s_add_i32 s95, s35, 0x180
	s_and_b64 s[40:41], s[38:39], exec
	ds_read_b128 v[0:3], v230
	ds_read_b128 v[4:7], v230 offset:1024
	ds_read_b128 v[12:15], v230 offset:2048
	ds_read_b128 v[16:19], v230 offset:3072
	s_cselect_b32 s40, s31, s95
	s_add_u32 s40, s8, s40
	s_addc_u32 s41, s9, 0
	s_add_i32 s95, s88, 0x80
	s_add_i32 s96, s93, 0x180
	s_and_b64 s[38:39], s[38:39], exec
	s_cselect_b32 s38, s95, s96
	s_add_u32 s38, s8, s38
	s_addc_u32 s39, s9, 0
	ds_read_b128 v[20:23], v231
	ds_read_b128 v[24:27], v231 offset:1024
	ds_read_b128 v[28:31], v231 offset:2048
	ds_read_b128 v[32:35], v231 offset:3072
	ds_read_b128 v[36:39], v231 offset:4096
	ds_read_b128 v[40:43], v231 offset:5120
	ds_read_b128 v[44:47], v231 offset:6144
	ds_read_b128 v[48:51], v231 offset:7168
	s_add_u32 s46, s46, 0x20000
	s_addc_u32 s47, s47, 0
	s_mov_b32 m0, s72
	s_nop 0
	global_load_lds_dwordx4 v213, s[46:47]
	s_mov_b32 m0, s78
	s_nop 0
	global_load_lds_dwordx4 v221, s[46:47]
	s_waitcnt lgkmcnt(8)
	s_barrier
	s_waitcnt lgkmcnt(0)
	s_setprio 1
	s_waitcnt lgkmcnt(6)
	v_mfma_scale_f32_16x16x128_f8f6f4 v[120:123], v[0:7], v[20:27], v[140:143], v232, v233 op_sel_hi:[0,0,0]
	v_mfma_scale_f32_16x16x128_f8f6f4 v[116:119], v[12:19], v[20:27], v[136:139], v232, v233 op_sel_hi:[0,0,0]
	s_waitcnt lgkmcnt(4)
	v_mfma_scale_f32_16x16x128_f8f6f4 v[104:107], v[0:7], v[28:35], v[140:143], v232, v233 op_sel_hi:[0,0,0]
	v_mfma_scale_f32_16x16x128_f8f6f4 v[100:103], v[12:19], v[28:35], v[136:139], v232, v233 op_sel_hi:[0,0,0]
	s_waitcnt lgkmcnt(2)
	v_mfma_scale_f32_16x16x128_f8f6f4 v[88:91], v[0:7], v[36:43], v[140:143], v232, v233 op_sel_hi:[0,0,0]
	v_mfma_scale_f32_16x16x128_f8f6f4 v[84:87], v[12:19], v[36:43], v[136:139], v232, v233 op_sel_hi:[0,0,0]
	s_waitcnt lgkmcnt(0)
	v_mfma_scale_f32_16x16x128_f8f6f4 v[72:75], v[0:7], v[44:51], v[140:143], v232, v233 op_sel_hi:[0,0,0]
	s_barrier
	v_mfma_scale_f32_16x16x128_f8f6f4 v[68:71], v[12:19], v[44:51], v[136:139], v232, v233 op_sel_hi:[0,0,0]
	s_setprio 0
	ds_read_b128 v[144:147], v234
	ds_read_b128 v[148:151], v234 offset:1024
	ds_read_b128 v[152:155], v234 offset:2048
	ds_read_b128 v[156:159], v234 offset:3072
	s_mov_b32 m0, s53
	s_nop 0
	global_load_lds_dwordx4 v215, s[44:45]
	s_mov_b32 m0, s54
	s_nop 0
	global_load_lds_dwordx4 v223, s[44:45]
	s_barrier
	s_waitcnt lgkmcnt(0)
	s_setprio 1
	s_waitcnt lgkmcnt(2)
	v_mfma_scale_f32_16x16x128_f8f6f4 v[124:127], v[144:151], v[20:27], v[128:131], v232, v233 op_sel_hi:[0,0,0]
	s_waitcnt lgkmcnt(0)
	v_mfma_scale_f32_16x16x128_f8f6f4 v[112:115], v[152:159], v[20:27], v[132:135], v232, v233 op_sel_hi:[0,0,0]
	v_mfma_scale_f32_16x16x128_f8f6f4 v[108:111], v[144:151], v[28:35], v[128:131], v232, v233 op_sel_hi:[0,0,0]
	v_mfma_scale_f32_16x16x128_f8f6f4 v[96:99], v[152:159], v[28:35], v[132:135], v232, v233 op_sel_hi:[0,0,0]
	v_mfma_scale_f32_16x16x128_f8f6f4 v[92:95], v[144:151], v[36:43], v[128:131], v232, v233 op_sel_hi:[0,0,0]
	v_mfma_scale_f32_16x16x128_f8f6f4 v[80:83], v[152:159], v[36:43], v[132:135], v232, v233 op_sel_hi:[0,0,0]
	v_mfma_scale_f32_16x16x128_f8f6f4 v[76:79], v[144:151], v[44:51], v[128:131], v232, v233 op_sel_hi:[0,0,0]
	s_barrier
	v_mfma_scale_f32_16x16x128_f8f6f4 v[64:67], v[152:159], v[44:51], v[132:135], v232, v233 op_sel_hi:[0,0,0]
	s_setprio 0
	ds_read_b128 v[28:31], v231 offset:16384
	ds_read_b128 v[32:35], v231 offset:17408
	ds_read_b128 v[160:163], v231 offset:18432
	ds_read_b128 v[164:167], v231 offset:19456
	ds_read_b128 v[168:171], v231 offset:20480
	ds_read_b128 v[172:175], v231 offset:21504
	ds_read_b128 v[176:179], v231 offset:22528
	ds_read_b128 v[180:183], v231 offset:23552
	s_mov_b32 m0, s52
	s_nop 0
	global_load_lds_dwordx4 v213, s[42:43]
	s_mov_b32 m0, s55
	s_nop 0
	global_load_lds_dwordx4 v221, s[42:43]
	s_barrier
	s_waitcnt lgkmcnt(0)
	s_setprio 1
	s_waitcnt lgkmcnt(6)
	v_mfma_scale_f32_16x16x128_f8f6f4 v[56:59], v[0:7], v[28:35], v[140:143], v232, v233 op_sel_hi:[0,0,0]
	v_mfma_scale_f32_16x16x128_f8f6f4 v[52:55], v[12:19], v[28:35], v[136:139], v232, v233 op_sel_hi:[0,0,0]
	s_waitcnt lgkmcnt(4)
	v_mfma_scale_f32_16x16x128_f8f6f4 v[40:43], v[0:7], v[160:167], v[140:143], v232, v233 op_sel_hi:[0,0,0]
	v_mfma_scale_f32_16x16x128_f8f6f4 v[36:39], v[12:19], v[160:167], v[136:139], v232, v233 op_sel_hi:[0,0,0]
	s_waitcnt lgkmcnt(2)
	v_mfma_scale_f32_16x16x128_f8f6f4 v[24:27], v[0:7], v[168:175], v[140:143], v232, v233 op_sel_hi:[0,0,0]
	v_mfma_scale_f32_16x16x128_f8f6f4 v[20:23], v[12:19], v[168:175], v[136:139], v232, v233 op_sel_hi:[0,0,0]
	s_waitcnt lgkmcnt(0)
	v_mfma_scale_f32_16x16x128_f8f6f4 v[8:11], v[0:7], v[176:183], v[140:143], v232, v233 op_sel_hi:[0,0,0]
	s_barrier
	v_mfma_scale_f32_16x16x128_f8f6f4 v[4:7], v[12:19], v[176:183], v[136:139], v232, v233 op_sel_hi:[0,0,0]
	s_setprio 0
	s_add_u32 s44, s44, 0x40000
	s_addc_u32 s45, s45, 0
	s_mov_b32 m0, s56
	s_nop 0
	global_load_lds_dwordx4 v215, s[44:45]
	s_mov_b32 m0, s57
	s_nop 0
	global_load_lds_dwordx4 v223, s[44:45]
	s_waitcnt vmcnt(6)
	s_barrier
	s_setprio 1
	v_mfma_scale_f32_16x16x128_f8f6f4 v[60:63], v[144:151], v[28:35], v[128:131], v232, v233 op_sel_hi:[0,0,0]
	v_mfma_scale_f32_16x16x128_f8f6f4 v[48:51], v[152:159], v[28:35], v[132:135], v232, v233 op_sel_hi:[0,0,0]
	v_mfma_scale_f32_16x16x128_f8f6f4 v[44:47], v[144:151], v[160:167], v[128:131], v232, v233 op_sel_hi:[0,0,0]
	v_mfma_scale_f32_16x16x128_f8f6f4 v[32:35], v[152:159], v[160:167], v[132:135], v232, v233 op_sel_hi:[0,0,0]
	v_mfma_scale_f32_16x16x128_f8f6f4 v[28:31], v[144:151], v[168:175], v[128:131], v232, v233 op_sel_hi:[0,0,0]
	v_mfma_scale_f32_16x16x128_f8f6f4 v[16:19], v[152:159], v[168:175], v[132:135], v232, v233 op_sel_hi:[0,0,0]
	v_mfma_scale_f32_16x16x128_f8f6f4 v[12:15], v[144:151], v[176:183], v[128:131], v232, v233 op_sel_hi:[0,0,0]
	s_barrier
	v_mfma_scale_f32_16x16x128_f8f6f4 v[0:3], v[152:159], v[176:183], v[132:135], v232, v233 op_sel_hi:[0,0,0]
	s_setprio 0
	ds_read_b128 v[128:131], v235
	ds_read_b128 v[132:135], v235 offset:1024
	ds_read_b128 v[136:139], v235 offset:2048
	ds_read_b128 v[140:143], v235 offset:3072
	ds_read_b128 v[144:147], v231 offset:32768
	ds_read_b128 v[148:151], v231 offset:33792
	ds_read_b128 v[152:155], v231 offset:34816
	ds_read_b128 v[156:159], v231 offset:35840
	ds_read_b128 v[160:163], v231 offset:36864
	ds_read_b128 v[164:167], v231 offset:37888
	ds_read_b128 v[168:171], v231 offset:38912
	ds_read_b128 v[172:175], v231 offset:39936
	s_add_u32 s42, s42, 0x20000
	s_addc_u32 s43, s43, 0
	s_mov_b32 m0, s58
	s_nop 0
	global_load_lds_dwordx4 v213, s[42:43]
	s_mov_b32 m0, s59
	s_nop 0
	global_load_lds_dwordx4 v221, s[42:43]
	s_waitcnt lgkmcnt(8)
	s_barrier
	s_waitcnt lgkmcnt(0)
	s_setprio 1
	s_waitcnt lgkmcnt(6)
	v_mfma_scale_f32_16x16x128_f8f6f4 v[120:123], v[128:135], v[144:151], v[120:123], v232, v233 op_sel_hi:[0,0,0]
	v_mfma_scale_f32_16x16x128_f8f6f4 v[116:119], v[136:143], v[144:151], v[116:119], v232, v233 op_sel_hi:[0,0,0]
	s_waitcnt lgkmcnt(4)
	v_mfma_scale_f32_16x16x128_f8f6f4 v[104:107], v[128:135], v[152:159], v[104:107], v232, v233 op_sel_hi:[0,0,0]
	v_mfma_scale_f32_16x16x128_f8f6f4 v[100:103], v[136:143], v[152:159], v[100:103], v232, v233 op_sel_hi:[0,0,0]
	s_waitcnt lgkmcnt(2)
	v_mfma_scale_f32_16x16x128_f8f6f4 v[88:91], v[128:135], v[160:167], v[88:91], v232, v233 op_sel_hi:[0,0,0]
	v_mfma_scale_f32_16x16x128_f8f6f4 v[84:87], v[136:143], v[160:167], v[84:87], v232, v233 op_sel_hi:[0,0,0]
	s_waitcnt lgkmcnt(0)
	v_mfma_scale_f32_16x16x128_f8f6f4 v[72:75], v[128:135], v[168:175], v[72:75], v232, v233 op_sel_hi:[0,0,0]
	s_barrier
	v_mfma_scale_f32_16x16x128_f8f6f4 v[68:71], v[136:143], v[168:175], v[68:71], v232, v233 op_sel_hi:[0,0,0]
	s_setprio 0
	ds_read_b128 v[176:179], v236
	ds_read_b128 v[180:183], v236 offset:1024
	ds_read_b128 v[184:187], v236 offset:2048
	ds_read_b128 v[188:191], v236 offset:3072
	s_mov_b32 m0, s60
	s_nop 0
	global_load_lds_dwordx4 v215, s[38:39]
	s_mov_b32 m0, s61
	s_nop 0
	global_load_lds_dwordx4 v223, s[38:39]
	s_barrier
	s_waitcnt lgkmcnt(0)
	s_setprio 1
	s_waitcnt lgkmcnt(2)
	v_mfma_scale_f32_16x16x128_f8f6f4 v[124:127], v[176:183], v[144:151], v[124:127], v232, v233 op_sel_hi:[0,0,0]
	s_waitcnt lgkmcnt(0)
	v_mfma_scale_f32_16x16x128_f8f6f4 v[112:115], v[184:191], v[144:151], v[112:115], v232, v233 op_sel_hi:[0,0,0]
	v_mfma_scale_f32_16x16x128_f8f6f4 v[108:111], v[176:183], v[152:159], v[108:111], v232, v233 op_sel_hi:[0,0,0]
	v_mfma_scale_f32_16x16x128_f8f6f4 v[96:99], v[184:191], v[152:159], v[96:99], v232, v233 op_sel_hi:[0,0,0]
	v_mfma_scale_f32_16x16x128_f8f6f4 v[92:95], v[176:183], v[160:167], v[92:95], v232, v233 op_sel_hi:[0,0,0]
	v_mfma_scale_f32_16x16x128_f8f6f4 v[80:83], v[184:191], v[160:167], v[80:83], v232, v233 op_sel_hi:[0,0,0]
	v_mfma_scale_f32_16x16x128_f8f6f4 v[76:79], v[176:183], v[168:175], v[76:79], v232, v233 op_sel_hi:[0,0,0]
	s_barrier
	v_mfma_scale_f32_16x16x128_f8f6f4 v[64:67], v[184:191], v[168:175], v[64:67], v232, v233 op_sel_hi:[0,0,0]
	s_setprio 0
	ds_read_b128 v[144:147], v231 offset:49152
	ds_read_b128 v[148:151], v231 offset:50176
	ds_read_b128 v[152:155], v231 offset:51200
	ds_read_b128 v[156:159], v231 offset:52224
	ds_read_b128 v[160:163], v231 offset:53248
	ds_read_b128 v[164:167], v231 offset:54272
	ds_read_b128 v[168:171], v231 offset:55296
	ds_read_b128 v[172:175], v231 offset:56320
	s_mov_b32 m0, s63
	s_nop 0
	global_load_lds_dwordx4 v213, s[40:41]
	s_mov_b32 m0, s64
	s_nop 0
	global_load_lds_dwordx4 v221, s[40:41]
	s_barrier
	s_waitcnt lgkmcnt(0)
	s_setprio 1
	s_waitcnt lgkmcnt(6)
	v_mfma_scale_f32_16x16x128_f8f6f4 v[56:59], v[128:135], v[144:151], v[56:59], v232, v233 op_sel_hi:[0,0,0]
	v_mfma_scale_f32_16x16x128_f8f6f4 v[52:55], v[136:143], v[144:151], v[52:55], v232, v233 op_sel_hi:[0,0,0]
	s_waitcnt lgkmcnt(4)
	v_mfma_scale_f32_16x16x128_f8f6f4 v[40:43], v[128:135], v[152:159], v[40:43], v232, v233 op_sel_hi:[0,0,0]
	v_mfma_scale_f32_16x16x128_f8f6f4 v[36:39], v[136:143], v[152:159], v[36:39], v232, v233 op_sel_hi:[0,0,0]
	s_waitcnt lgkmcnt(2)
	v_mfma_scale_f32_16x16x128_f8f6f4 v[24:27], v[128:135], v[160:167], v[24:27], v232, v233 op_sel_hi:[0,0,0]
	v_mfma_scale_f32_16x16x128_f8f6f4 v[20:23], v[136:143], v[160:167], v[20:23], v232, v233 op_sel_hi:[0,0,0]
	s_waitcnt lgkmcnt(0)
	v_mfma_scale_f32_16x16x128_f8f6f4 v[8:11], v[128:135], v[168:175], v[8:11], v232, v233 op_sel_hi:[0,0,0]
	s_barrier
	v_mfma_scale_f32_16x16x128_f8f6f4 v[4:7], v[136:143], v[168:175], v[4:7], v232, v233 op_sel_hi:[0,0,0]
	s_setprio 0
	s_add_u32 s38, s38, 0x40000
	s_addc_u32 s39, s39, 0
	s_mov_b32 m0, s65
	s_nop 0
	global_load_lds_dwordx4 v215, s[38:39]
	s_mov_b32 m0, s66
	s_nop 0
	global_load_lds_dwordx4 v223, s[38:39]
	s_waitcnt vmcnt(6)
	s_barrier
	s_setprio 1
	v_mfma_scale_f32_16x16x128_f8f6f4 v[60:63], v[176:183], v[144:151], v[60:63], v232, v233 op_sel_hi:[0,0,0]
	v_mfma_scale_f32_16x16x128_f8f6f4 v[48:51], v[184:191], v[144:151], v[48:51], v232, v233 op_sel_hi:[0,0,0]
	v_mfma_scale_f32_16x16x128_f8f6f4 v[44:47], v[176:183], v[152:159], v[44:47], v232, v233 op_sel_hi:[0,0,0]
	v_mfma_scale_f32_16x16x128_f8f6f4 v[32:35], v[184:191], v[152:159], v[32:35], v232, v233 op_sel_hi:[0,0,0]
	v_mfma_scale_f32_16x16x128_f8f6f4 v[28:31], v[176:183], v[160:167], v[28:31], v232, v233 op_sel_hi:[0,0,0]
	v_mfma_scale_f32_16x16x128_f8f6f4 v[16:19], v[184:191], v[160:167], v[16:19], v232, v233 op_sel_hi:[0,0,0]
	v_mfma_scale_f32_16x16x128_f8f6f4 v[12:15], v[176:183], v[168:175], v[12:15], v232, v233 op_sel_hi:[0,0,0]
	s_barrier
	v_mfma_scale_f32_16x16x128_f8f6f4 v[0:3], v[184:191], v[168:175], v[0:3], v232, v233 op_sel_hi:[0,0,0]
	s_setprio 0
	s_cmp_lt_i32 s94, 3
	s_cbranch_scc1 .LBB2_36
	s_lshl_b32 s39, s27, 7
	s_lshl_b32 s40, s91, 3
	s_lshl_b32 s38, s30, 9
	s_add_i32 s39, s39, s40
	s_add_i32 s38, s38, s39
	s_ashr_i32 s39, s38, 31
	s_lshl_b64 s[38:39], s[38:39], 13
	s_add_u32 s38, s2, s38
	s_addc_u32 s39, s3, s39
	s_mov_b32 s97, 4
	s_movk_i32 s96, 0x280
	s_branch .LBB2_34
.LBB2_33:
	s_add_i32 s98, s97, -2
	s_cmp_lt_u32 s98, 8
	s_cselect_b32 s42, s35, s92
	s_add_i32 s42, s42, s96
	s_addk_i32 s42, 0xff00
	s_add_u32 s99, s8, s42
	s_addc_u32 vcc_lo, s9, 0
	s_cmp_lt_u32 s98, 6
	s_cselect_b32 s42, s35, s92
	s_add_i32 s42, s42, s96
	s_add_i32 s44, s42, 0xffffff80
	s_and_b64 s[42:43], s[40:41], exec
	s_cselect_b32 s42, s90, s44
	s_add_u32 s44, s8, s42
	s_addc_u32 s45, s9, 0
	s_add_i32 vcc_hi, s93, s96
	s_add_i32 s46, vcc_hi, 0xffffff80
	s_and_b64 s[42:43], s[40:41], exec
	s_cselect_b32 s42, s88, s46
	s_add_u32 s46, s8, s42
	s_addc_u32 s47, s9, 0
	s_cmp_lt_u32 s98, 5
	s_cselect_b32 s42, s35, s92
	s_add_i32 s98, s42, s96
	s_and_b64 s[42:43], s[40:41], exec
	ds_read_b128 v[128:131], v230
	ds_read_b128 v[132:135], v230 offset:1024
	ds_read_b128 v[136:139], v230 offset:2048
	ds_read_b128 v[140:143], v230 offset:3072
	s_cselect_b32 s42, s31, s98
	s_add_u32 s42, s8, s42
	s_addc_u32 s43, s9, 0
	s_and_b64 s[40:41], s[40:41], exec
	s_cselect_b32 s40, s95, vcc_hi
	s_add_u32 s40, s8, s40
	s_addc_u32 s41, s9, 0
	ds_read_b128 v[144:147], v231
	ds_read_b128 v[148:151], v231 offset:1024
	ds_read_b128 v[152:155], v231 offset:2048
	ds_read_b128 v[156:159], v231 offset:3072
	ds_read_b128 v[160:163], v231 offset:4096
	ds_read_b128 v[164:167], v231 offset:5120
	ds_read_b128 v[168:171], v231 offset:6144
	ds_read_b128 v[172:175], v231 offset:7168
	s_add_u32 s98, s99, 0x20000
	s_addc_u32 s99, vcc_lo, 0
	s_mov_b32 m0, s72
	s_nop 0
	global_load_lds_dwordx4 v213, s[98:99]
	s_mov_b32 m0, s78
	s_nop 0
	global_load_lds_dwordx4 v221, s[98:99]
	s_waitcnt lgkmcnt(8)
	s_barrier
	s_waitcnt lgkmcnt(0)
	s_setprio 1
	s_waitcnt lgkmcnt(6)
	v_mfma_scale_f32_16x16x128_f8f6f4 v[120:123], v[128:135], v[144:151], v[120:123], v232, v233 op_sel_hi:[0,0,0]
	v_mfma_scale_f32_16x16x128_f8f6f4 v[116:119], v[136:143], v[144:151], v[116:119], v232, v233 op_sel_hi:[0,0,0]
	s_waitcnt lgkmcnt(4)
	v_mfma_scale_f32_16x16x128_f8f6f4 v[104:107], v[128:135], v[152:159], v[104:107], v232, v233 op_sel_hi:[0,0,0]
	v_mfma_scale_f32_16x16x128_f8f6f4 v[100:103], v[136:143], v[152:159], v[100:103], v232, v233 op_sel_hi:[0,0,0]
	s_waitcnt lgkmcnt(2)
	v_mfma_scale_f32_16x16x128_f8f6f4 v[88:91], v[128:135], v[160:167], v[88:91], v232, v233 op_sel_hi:[0,0,0]
	v_mfma_scale_f32_16x16x128_f8f6f4 v[84:87], v[136:143], v[160:167], v[84:87], v232, v233 op_sel_hi:[0,0,0]
	s_waitcnt lgkmcnt(0)
	v_mfma_scale_f32_16x16x128_f8f6f4 v[72:75], v[128:135], v[168:175], v[72:75], v232, v233 op_sel_hi:[0,0,0]
	s_barrier
	v_mfma_scale_f32_16x16x128_f8f6f4 v[68:71], v[136:143], v[168:175], v[68:71], v232, v233 op_sel_hi:[0,0,0]
	s_setprio 0
	ds_read_b128 v[176:179], v234
	ds_read_b128 v[180:183], v234 offset:1024
	ds_read_b128 v[184:187], v234 offset:2048
	ds_read_b128 v[188:191], v234 offset:3072
	s_mov_b32 m0, s53
	s_nop 0
	global_load_lds_dwordx4 v215, s[46:47]
	s_mov_b32 m0, s54
	s_nop 0
	global_load_lds_dwordx4 v223, s[46:47]
	s_barrier
	s_waitcnt lgkmcnt(0)
	s_setprio 1
	s_waitcnt lgkmcnt(2)
	v_mfma_scale_f32_16x16x128_f8f6f4 v[124:127], v[176:183], v[144:151], v[124:127], v232, v233 op_sel_hi:[0,0,0]
	s_waitcnt lgkmcnt(0)
	v_mfma_scale_f32_16x16x128_f8f6f4 v[112:115], v[184:191], v[144:151], v[112:115], v232, v233 op_sel_hi:[0,0,0]
	v_mfma_scale_f32_16x16x128_f8f6f4 v[108:111], v[176:183], v[152:159], v[108:111], v232, v233 op_sel_hi:[0,0,0]
	v_mfma_scale_f32_16x16x128_f8f6f4 v[96:99], v[184:191], v[152:159], v[96:99], v232, v233 op_sel_hi:[0,0,0]
	v_mfma_scale_f32_16x16x128_f8f6f4 v[92:95], v[176:183], v[160:167], v[92:95], v232, v233 op_sel_hi:[0,0,0]
	v_mfma_scale_f32_16x16x128_f8f6f4 v[80:83], v[184:191], v[160:167], v[80:83], v232, v233 op_sel_hi:[0,0,0]
	v_mfma_scale_f32_16x16x128_f8f6f4 v[76:79], v[176:183], v[168:175], v[76:79], v232, v233 op_sel_hi:[0,0,0]
	s_barrier
	v_mfma_scale_f32_16x16x128_f8f6f4 v[64:67], v[184:191], v[168:175], v[64:67], v232, v233 op_sel_hi:[0,0,0]
	s_setprio 0
	ds_read_b128 v[144:147], v231 offset:16384
	ds_read_b128 v[148:151], v231 offset:17408
	ds_read_b128 v[152:155], v231 offset:18432
	ds_read_b128 v[156:159], v231 offset:19456
	ds_read_b128 v[160:163], v231 offset:20480
	ds_read_b128 v[164:167], v231 offset:21504
	ds_read_b128 v[168:171], v231 offset:22528
	ds_read_b128 v[172:175], v231 offset:23552
	s_mov_b32 m0, s52
	s_nop 0
	global_load_lds_dwordx4 v213, s[44:45]
	s_mov_b32 m0, s55
	s_nop 0
	global_load_lds_dwordx4 v221, s[44:45]
	s_barrier
	s_waitcnt lgkmcnt(0)
	s_setprio 1
	s_waitcnt lgkmcnt(6)
	v_mfma_scale_f32_16x16x128_f8f6f4 v[56:59], v[128:135], v[144:151], v[56:59], v232, v233 op_sel_hi:[0,0,0]
	v_mfma_scale_f32_16x16x128_f8f6f4 v[52:55], v[136:143], v[144:151], v[52:55], v232, v233 op_sel_hi:[0,0,0]
	s_waitcnt lgkmcnt(4)
	v_mfma_scale_f32_16x16x128_f8f6f4 v[40:43], v[128:135], v[152:159], v[40:43], v232, v233 op_sel_hi:[0,0,0]
	v_mfma_scale_f32_16x16x128_f8f6f4 v[36:39], v[136:143], v[152:159], v[36:39], v232, v233 op_sel_hi:[0,0,0]
	s_waitcnt lgkmcnt(2)
	v_mfma_scale_f32_16x16x128_f8f6f4 v[24:27], v[128:135], v[160:167], v[24:27], v232, v233 op_sel_hi:[0,0,0]
	v_mfma_scale_f32_16x16x128_f8f6f4 v[20:23], v[136:143], v[160:167], v[20:23], v232, v233 op_sel_hi:[0,0,0]
	s_waitcnt lgkmcnt(0)
	v_mfma_scale_f32_16x16x128_f8f6f4 v[8:11], v[128:135], v[168:175], v[8:11], v232, v233 op_sel_hi:[0,0,0]
	s_barrier
	v_mfma_scale_f32_16x16x128_f8f6f4 v[4:7], v[136:143], v[168:175], v[4:7], v232, v233 op_sel_hi:[0,0,0]
	s_setprio 0
	s_add_u32 s46, s46, 0x40000
	s_addc_u32 s47, s47, 0
	s_mov_b32 m0, s56
	s_nop 0
	global_load_lds_dwordx4 v215, s[46:47]
	s_mov_b32 m0, s57
	s_nop 0
	global_load_lds_dwordx4 v223, s[46:47]
	s_waitcnt vmcnt(6)
	s_barrier
	s_setprio 1
	v_mfma_scale_f32_16x16x128_f8f6f4 v[60:63], v[176:183], v[144:151], v[60:63], v232, v233 op_sel_hi:[0,0,0]
	v_mfma_scale_f32_16x16x128_f8f6f4 v[48:51], v[184:191], v[144:151], v[48:51], v232, v233 op_sel_hi:[0,0,0]
	v_mfma_scale_f32_16x16x128_f8f6f4 v[44:47], v[176:183], v[152:159], v[44:47], v232, v233 op_sel_hi:[0,0,0]
	v_mfma_scale_f32_16x16x128_f8f6f4 v[32:35], v[184:191], v[152:159], v[32:35], v232, v233 op_sel_hi:[0,0,0]
	v_mfma_scale_f32_16x16x128_f8f6f4 v[28:31], v[176:183], v[160:167], v[28:31], v232, v233 op_sel_hi:[0,0,0]
	v_mfma_scale_f32_16x16x128_f8f6f4 v[16:19], v[184:191], v[160:167], v[16:19], v232, v233 op_sel_hi:[0,0,0]
	v_mfma_scale_f32_16x16x128_f8f6f4 v[12:15], v[176:183], v[168:175], v[12:15], v232, v233 op_sel_hi:[0,0,0]
	s_barrier
	v_mfma_scale_f32_16x16x128_f8f6f4 v[0:3], v[184:191], v[168:175], v[0:3], v232, v233 op_sel_hi:[0,0,0]
	s_setprio 0
	ds_read_b128 v[128:131], v235
	ds_read_b128 v[132:135], v235 offset:1024
	ds_read_b128 v[136:139], v235 offset:2048
	ds_read_b128 v[140:143], v235 offset:3072
	ds_read_b128 v[144:147], v231 offset:32768
	ds_read_b128 v[148:151], v231 offset:33792
	ds_read_b128 v[152:155], v231 offset:34816
	ds_read_b128 v[156:159], v231 offset:35840
	ds_read_b128 v[160:163], v231 offset:36864
	ds_read_b128 v[164:167], v231 offset:37888
	ds_read_b128 v[168:171], v231 offset:38912
	ds_read_b128 v[172:175], v231 offset:39936
	s_add_u32 s44, s44, 0x20000
	s_addc_u32 s45, s45, 0
	s_mov_b32 m0, s58
	s_nop 0
	global_load_lds_dwordx4 v213, s[44:45]
	s_mov_b32 m0, s59
	s_nop 0
	global_load_lds_dwordx4 v221, s[44:45]
	s_waitcnt lgkmcnt(8)
	s_barrier
	s_waitcnt lgkmcnt(0)
	s_setprio 1
	s_waitcnt lgkmcnt(6)
	v_mfma_scale_f32_16x16x128_f8f6f4 v[120:123], v[128:135], v[144:151], v[120:123], v232, v233 op_sel_hi:[0,0,0]
	v_mfma_scale_f32_16x16x128_f8f6f4 v[116:119], v[136:143], v[144:151], v[116:119], v232, v233 op_sel_hi:[0,0,0]
	s_waitcnt lgkmcnt(4)
	v_mfma_scale_f32_16x16x128_f8f6f4 v[104:107], v[128:135], v[152:159], v[104:107], v232, v233 op_sel_hi:[0,0,0]
	v_mfma_scale_f32_16x16x128_f8f6f4 v[100:103], v[136:143], v[152:159], v[100:103], v232, v233 op_sel_hi:[0,0,0]
	s_waitcnt lgkmcnt(2)
	v_mfma_scale_f32_16x16x128_f8f6f4 v[88:91], v[128:135], v[160:167], v[88:91], v232, v233 op_sel_hi:[0,0,0]
	v_mfma_scale_f32_16x16x128_f8f6f4 v[84:87], v[136:143], v[160:167], v[84:87], v232, v233 op_sel_hi:[0,0,0]
	s_waitcnt lgkmcnt(0)
	v_mfma_scale_f32_16x16x128_f8f6f4 v[72:75], v[128:135], v[168:175], v[72:75], v232, v233 op_sel_hi:[0,0,0]
	s_barrier
	v_mfma_scale_f32_16x16x128_f8f6f4 v[68:71], v[136:143], v[168:175], v[68:71], v232, v233 op_sel_hi:[0,0,0]
	s_setprio 0
	ds_read_b128 v[176:179], v236
	ds_read_b128 v[180:183], v236 offset:1024
	ds_read_b128 v[184:187], v236 offset:2048
	ds_read_b128 v[188:191], v236 offset:3072
	s_mov_b32 m0, s60
	s_nop 0
	global_load_lds_dwordx4 v215, s[40:41]
	s_mov_b32 m0, s61
	s_nop 0
	global_load_lds_dwordx4 v223, s[40:41]
	s_barrier
	s_waitcnt lgkmcnt(0)
	s_setprio 1
	s_waitcnt lgkmcnt(2)
	v_mfma_scale_f32_16x16x128_f8f6f4 v[124:127], v[176:183], v[144:151], v[124:127], v232, v233 op_sel_hi:[0,0,0]
	s_waitcnt lgkmcnt(0)
	v_mfma_scale_f32_16x16x128_f8f6f4 v[112:115], v[184:191], v[144:151], v[112:115], v232, v233 op_sel_hi:[0,0,0]
	v_mfma_scale_f32_16x16x128_f8f6f4 v[108:111], v[176:183], v[152:159], v[108:111], v232, v233 op_sel_hi:[0,0,0]
	v_mfma_scale_f32_16x16x128_f8f6f4 v[96:99], v[184:191], v[152:159], v[96:99], v232, v233 op_sel_hi:[0,0,0]
	v_mfma_scale_f32_16x16x128_f8f6f4 v[92:95], v[176:183], v[160:167], v[92:95], v232, v233 op_sel_hi:[0,0,0]
	v_mfma_scale_f32_16x16x128_f8f6f4 v[80:83], v[184:191], v[160:167], v[80:83], v232, v233 op_sel_hi:[0,0,0]
	v_mfma_scale_f32_16x16x128_f8f6f4 v[76:79], v[176:183], v[168:175], v[76:79], v232, v233 op_sel_hi:[0,0,0]
	s_barrier
	v_mfma_scale_f32_16x16x128_f8f6f4 v[64:67], v[184:191], v[168:175], v[64:67], v232, v233 op_sel_hi:[0,0,0]
	s_setprio 0
	ds_read_b128 v[144:147], v231 offset:49152
	ds_read_b128 v[148:151], v231 offset:50176
	ds_read_b128 v[152:155], v231 offset:51200
	ds_read_b128 v[156:159], v231 offset:52224
	ds_read_b128 v[160:163], v231 offset:53248
	ds_read_b128 v[164:167], v231 offset:54272
	ds_read_b128 v[168:171], v231 offset:55296
	ds_read_b128 v[172:175], v231 offset:56320
	s_mov_b32 m0, s63
	s_nop 0
	global_load_lds_dwordx4 v213, s[42:43]
	s_mov_b32 m0, s64
	s_nop 0
	global_load_lds_dwordx4 v221, s[42:43]
	s_barrier
	s_waitcnt lgkmcnt(0)
	s_setprio 1
	s_waitcnt lgkmcnt(6)
	v_mfma_scale_f32_16x16x128_f8f6f4 v[56:59], v[128:135], v[144:151], v[56:59], v232, v233 op_sel_hi:[0,0,0]
	v_mfma_scale_f32_16x16x128_f8f6f4 v[52:55], v[136:143], v[144:151], v[52:55], v232, v233 op_sel_hi:[0,0,0]
	s_waitcnt lgkmcnt(4)
	v_mfma_scale_f32_16x16x128_f8f6f4 v[40:43], v[128:135], v[152:159], v[40:43], v232, v233 op_sel_hi:[0,0,0]
	v_mfma_scale_f32_16x16x128_f8f6f4 v[36:39], v[136:143], v[152:159], v[36:39], v232, v233 op_sel_hi:[0,0,0]
	s_waitcnt lgkmcnt(2)
	v_mfma_scale_f32_16x16x128_f8f6f4 v[24:27], v[128:135], v[160:167], v[24:27], v232, v233 op_sel_hi:[0,0,0]
	v_mfma_scale_f32_16x16x128_f8f6f4 v[20:23], v[136:143], v[160:167], v[20:23], v232, v233 op_sel_hi:[0,0,0]
	s_waitcnt lgkmcnt(0)
	v_mfma_scale_f32_16x16x128_f8f6f4 v[8:11], v[128:135], v[168:175], v[8:11], v232, v233 op_sel_hi:[0,0,0]
	s_barrier
	v_mfma_scale_f32_16x16x128_f8f6f4 v[4:7], v[136:143], v[168:175], v[4:7], v232, v233 op_sel_hi:[0,0,0]
	s_setprio 0
	s_add_u32 s40, s40, 0x40000
	s_addc_u32 s41, s41, 0
	s_mov_b32 m0, s65
	s_nop 0
	global_load_lds_dwordx4 v215, s[40:41]
	s_mov_b32 m0, s66
	s_nop 0
	global_load_lds_dwordx4 v223, s[40:41]
	s_waitcnt vmcnt(6)
	s_barrier
	s_setprio 1
	v_mfma_scale_f32_16x16x128_f8f6f4 v[60:63], v[176:183], v[144:151], v[60:63], v232, v233 op_sel_hi:[0,0,0]
	v_mfma_scale_f32_16x16x128_f8f6f4 v[48:51], v[184:191], v[144:151], v[48:51], v232, v233 op_sel_hi:[0,0,0]
	v_mfma_scale_f32_16x16x128_f8f6f4 v[44:47], v[176:183], v[152:159], v[44:47], v232, v233 op_sel_hi:[0,0,0]
	v_mfma_scale_f32_16x16x128_f8f6f4 v[32:35], v[184:191], v[152:159], v[32:35], v232, v233 op_sel_hi:[0,0,0]
	v_mfma_scale_f32_16x16x128_f8f6f4 v[28:31], v[176:183], v[160:167], v[28:31], v232, v233 op_sel_hi:[0,0,0]
	v_mfma_scale_f32_16x16x128_f8f6f4 v[16:19], v[184:191], v[160:167], v[16:19], v232, v233 op_sel_hi:[0,0,0]
	v_mfma_scale_f32_16x16x128_f8f6f4 v[12:15], v[176:183], v[168:175], v[12:15], v232, v233 op_sel_hi:[0,0,0]
	s_barrier
	v_mfma_scale_f32_16x16x128_f8f6f4 v[0:3], v[184:191], v[168:175], v[0:3], v232, v233 op_sel_hi:[0,0,0]
	s_setprio 0
	s_add_i32 s40, s97, 2
	s_addk_i32 s96, 0x100
	s_cmp_ge_i32 s97, s94
	s_mov_b32 s97, s40
	s_cbranch_scc1 .LBB2_36
